# v46_poll2
# baseline (speedup 1.0000x reference)
.LBB3_184:
	s_or_b64 exec, exec, s[4:5]
	v_cndmask_b32_e64 v4, 0, 1, s[6:7]
	v_cmp_ne_u32_e32 vcc, 0, v4
	s_cmp_eq_u64 vcc, exec
	s_cbranch_scc1 .LBB3_181
	s_mov_b64 s[6:7], -1
	s_sleep 2
	s_and_saveexec_b64 s[4:5], s[0:1]
	s_cbranch_execz .LBB3_187
	global_load_dword v4, v[2:3], off sc1
	s_waitcnt vmcnt(0)
	v_cmp_ne_u32_e32 vcc, 0, v4
	s_orn2_b64 s[6:7], vcc, exec

.LBB3_193:
	s_or_b64 exec, exec, s[4:5]
	v_cndmask_b32_e64 v4, 0, 1, s[6:7]
	v_cmp_ne_u32_e32 vcc, 0, v4
	s_cmp_eq_u64 vcc, exec
	s_cbranch_scc1 .LBB3_181
	s_add_i32 s11, s11, -4
	s_cmp_eq_u32 s11, 0
	s_cselect_b64 s[2:3], -1, 0
	s_sleep 2
	s_branch .LBB3_181
